# v69 + P1 BRP dot loop (second copy): 16 loads in flight with counted waits instead of load,load,wait per term
# baseline (speedup 1.0000x reference)
; __device__ __forceinline__ void ph1_small(const Args& a, int tid, int wave, int lane, int G, int bid) {
;     ...
;         for (int o = (wave == 2 ? bid : NB * NEXP); o < NB * NEXP; o += G) { const int b = o >> 5, e = o & 31; float s = 0.f;
; #pragma unroll 8
;             for (int k = lane; k < DM; k += 64) s += MOD[(size_t)b * MODW + 3 * DM + k] * wr[k * 32 + e];
;             s = wave_sum(s); if (lane == 0) BRP[o] = s + br[e]; }
.LBB0_317:
	global_load_dword v39, v[20:21], off offset:-1792
	global_load_dword v56, v[20:21], off offset:-1536
	global_load_dword v57, v[20:21], off offset:-1280
	global_load_dword v58, v[20:21], off offset:-1024
	global_load_dword v59, v[20:21], off offset:-768
	global_load_dword v60, v[20:21], off offset:-512
	global_load_dword v61, v[20:21], off offset:-256
	global_load_dword v62, v[20:21], off
	global_load_dword v40, v18, s[44:45]
	global_load_dword v41, v16, s[44:45]
	global_load_dword v42, v14, s[44:45]
	global_load_dword v43, v12, s[44:45]
	global_load_dword v44, v10, s[44:45]
	global_load_dword v45, v8, s[44:45]
	global_load_dword v46, v6, s[44:45]
	global_load_dword v47, v2, s[44:45]
	v_add_u32_e32 v38, 0x200, v38
	s_add_u32 s44, s44, 0x10000
	s_movk_i32 s41, 0x5ff
	s_addc_u32 s45, s45, 0
	v_cmp_lt_u32_e32 vcc, s41, v38
	v_lshl_add_u64 v[20:21], v[20:21], 0, s[46:47]
	s_or_b64 s[42:43], vcc, s[42:43]
	s_waitcnt vmcnt(7)
	v_fmac_f32_e32 v37, v39, v40
	s_waitcnt vmcnt(6)
	v_fmac_f32_e32 v37, v56, v41
	s_waitcnt vmcnt(5)
	v_fmac_f32_e32 v37, v57, v42
	s_waitcnt vmcnt(4)
	v_fmac_f32_e32 v37, v58, v43
	s_waitcnt vmcnt(3)
	v_fmac_f32_e32 v37, v59, v44
	s_waitcnt vmcnt(2)
	v_fmac_f32_e32 v37, v60, v45
	s_waitcnt vmcnt(1)
	v_fmac_f32_e32 v37, v61, v46
	s_waitcnt vmcnt(0)
	v_fmac_f32_e32 v37, v62, v47
	s_andn2_b64 exec, exec, s[42:43]
	s_cbranch_execnz .LBB0_317
	s_or_b64 exec, exec, s[42:43]
	ds_bpermute_b32 v2, v22, v37
	s_waitcnt lgkmcnt(0)
	v_add_f32_e32 v2, v37, v2
	ds_bpermute_b32 v6, v23, v2
	s_waitcnt lgkmcnt(0)
	v_add_f32_e32 v2, v2, v6
	ds_bpermute_b32 v6, v24, v2
	s_waitcnt lgkmcnt(0)
	v_add_f32_e32 v2, v2, v6
	ds_bpermute_b32 v6, v25, v2
	s_waitcnt lgkmcnt(0)
	v_add_f32_e32 v2, v2, v6
	ds_bpermute_b32 v6, v26, v2
	s_waitcnt lgkmcnt(0)
	v_add_f32_e32 v2, v2, v6
	ds_bpermute_b32 v6, v27, v2
	s_and_saveexec_b64 s[42:43], s[36:37]
	s_cbranch_execz .LBB0_315
	s_and_b32 s41, s40, 31
	s_lshl_b32 s41, s41, 2
	v_readlane_b32 s0, v250, 60
	v_mov_b32_e32 v7, s41
	v_readlane_b32 s14, v251, 10
	v_readlane_b32 s15, v251, 11
	s_ashr_i32 s41, s40, 31
	s_lshl_b64 s[44:45], s[40:41], 2
	s_waitcnt lgkmcnt(0)
	v_add_f32_e32 v2, v2, v6
	s_add_u32 s44, s89, s44
	v_readlane_b32 s0, v250, 57
	global_load_dword v7, v7, s[14:15]
	s_addc_u32 s45, s0, s45
	v_readlane_b32 s1, v250, 61
	v_readlane_b32 s2, v250, 62
	v_readlane_b32 s3, v250, 63
	v_readlane_b32 s4, v251, 0
	v_readlane_b32 s5, v251, 1
	v_readlane_b32 s6, v251, 2
	v_readlane_b32 s7, v251, 3
	v_readlane_b32 s8, v251, 4
	v_readlane_b32 s9, v251, 5
	v_readlane_b32 s10, v251, 6
	v_readlane_b32 s11, v251, 7
	v_readlane_b32 s12, v251, 8
	v_readlane_b32 s13, v251, 9
	s_waitcnt vmcnt(0)
	v_add_f32_e32 v2, v2, v7
	global_store_dword v3, v2, s[44:45]
	s_branch .LBB0_315
